# prologue x->bf16 row loop: gain loads hoisted out of the row loop, all x loads of a row issued at the loop top
# baseline (speedup 1.0000x reference)
; __global__ void __launch_bounds__(NWAVES * 64, 2) mk_fwd(Args a) {
;     ...
;         for (int row = gw; row < NT; row += ngw) { const float* xr = a.in[0] + (size_t)row * DM; float sq = 0.f;
; #pragma unroll
;             for (int j = 0; j < 4; ++j) { const f32x4 v0 = *(const f32x4*)(xr + (lane + 64 * j) * 8), v1 = *(const f32x4*)(xr + (lane + 64 * j) * 8 + 4);
;                 const f32x4 g0 = *(const f32x4*)(a.in[2] + (lane + 64 * j) * 8), g1 = *(const f32x4*)(a.in[2] + (lane + 64 * j) * 8 + 4);
.LBB0_74:
.LBB0_75:
	s_ashr_i32 s97, s96, 31
	s_lshl_b64 s[0:1], s[96:97], 3
	s_add_u32 s3, s0, 0x74000
	s_addc_u32 s12, s1, 0
	s_ashr_i32 s59, s58, 31
	s_lshl_b64 s[0:1], s[96:97], 12
	v_readlane_b32 s36, v247, 3
	s_lshl_b64 s[4:5], s[58:59], 3
	s_waitcnt vmcnt(0)
	v_lshl_or_b32 v10, v194, 4, s0
	v_mov_b32_e32 v11, s1
	s_lshl_b64 s[6:7], s[58:59], 12
	s_lshl_b64 s[0:1], s[96:97], 13
	v_readlane_b32 s37, v247, 4
	s_add_u32 s0, s36, s0
	v_lshlrev_b32_e32 v2, 5, v194
	v_mov_b32_e32 v3, 0
	v_readlane_b32 s40, v247, 7
	v_readlane_b32 s41, v247, 8
	s_addc_u32 s1, s37, s1
	v_or_b32_e32 v6, 0x1000, v2
	v_lshl_add_u64 v[4:5], s[40:41], 0, v[2:3]
	v_or_b32_e32 v8, 0x1800, v2
	v_lshl_add_u64 v[12:13], s[0:1], 0, v[2:3]
	v_mbcnt_lo_u32_b32 v2, -1, 0
	v_mbcnt_hi_u32_b32 v2, -1, v2
	v_mov_b32_e32 v7, v3
	v_mov_b32_e32 v9, v3
	s_mov_b64 s[0:1], 0x1000
	v_and_b32_e32 v14, 64, v2
	v_cmp_eq_u32_e32 vcc, 0, v194
	v_lshl_add_u64 v[6:7], s[40:41], 0, v[6:7]
	v_lshl_add_u64 v[8:9], s[40:41], 0, v[8:9]
	v_lshl_add_u64 v[12:13], v[12:13], 0, s[0:1]
	s_lshl_b64 s[10:11], s[58:59], 13
	s_mov_b32 s13, 0x3be00000
	v_add_u32_e32 v16, 64, v14
	v_xor_b32_e32 v17, 1, v2
	v_xor_b32_e32 v18, 2, v2
	v_xor_b32_e32 v19, 4, v2
	v_xor_b32_e32 v20, 8, v2
	v_xor_b32_e32 v21, 16, v2
	v_xor_b32_e32 v22, 32, v2
	s_mov_b32 s14, s96
	v_readlane_b32 s38, v247, 5
	v_readlane_b32 s39, v247, 6
	v_readlane_b32 s42, v247, 9
	v_readlane_b32 s43, v247, 10
	v_readlane_b32 s44, v247, 11
	v_readlane_b32 s45, v247, 12
	v_readlane_b32 s46, v247, 13
	v_readlane_b32 s47, v247, 14
	v_readlane_b32 s48, v247, 15
	v_readlane_b32 s49, v247, 16
	v_readlane_b32 s50, v247, 17
	v_readlane_b32 s51, v247, 18
	global_load_dwordx4 v[220:223], v[4:5], off
	global_load_dwordx4 v[224:227], v[4:5], off offset:16
	global_load_dwordx4 v[228:231], v[4:5], off offset:2048
	global_load_dwordx4 v[232:235], v[4:5], off offset:2064
	global_load_dwordx4 v[236:239], v[6:7], off
	global_load_dwordx4 v[240:243], v[6:7], off offset:16
	global_load_dwordx4 v[248:251], v[8:9], off
	global_load_dwordx4 v[252:255], v[8:9], off offset:16
	s_waitcnt vmcnt(0)
	s_branch .LBB0_77

; __device__ __forceinline__ u32x4 pack8(f32x4 v0, f32x4 v1) { u32x4 w; w.x = cvt_pk_bf16(v0[0], v0[1]); w.y = cvt_pk_bf16(v0[2], v0[3]); w.z = cvt_pk_bf16(v1[0], v1[1]); w.w = cvt_pk_bf16(v1[2], v1[3]); return w; }
; __device__ __forceinline__ float sum8sq(f32x4 a, f32x4 b) { return (a[0] * a[0] + a[1] * a[1]) + (a[2] * a[2] + a[3] * a[3]) + (b[0] * b[0] + b[1] * b[1]) + (b[2] * b[2] + b[3] * b[3]); }
; __device__ __forceinline__ ss_t ss_fix(float sq) { return (ss_t)(sq * 16777216.f); }
; __global__ void __launch_bounds__(NWAVES * 64, 2) mk_fwd(Args a) {
;     ...
;         for (int row = gw; row < NT; row += ngw) { const float* xr = a.in[0] + (size_t)row * DM; float sq = 0.f;
; #pragma unroll
;             for (int j = 0; j < 4; ++j) { const f32x4 v0 = *(const f32x4*)(xr + (lane + 64 * j) * 8), v1 = *(const f32x4*)(xr + (lane + 64 * j) * 8 + 4);
;                 const f32x4 g0 = *(const f32x4*)(a.in[2] + (lane + 64 * j) * 8), g1 = *(const f32x4*)(a.in[2] + (lane + 64 * j) * 8 + 4);
;                 *(u32x4*)(XBA + (size_t)row * DM + (lane + 64 * j) * 8) = epi::pack8(v0 * g0, v1 * g1); sq += epi::sum8sq(v0, v1); }
;             sq = wave_sum(sq); if (lane == 0) ssbase[7 * NT + row] = epi::ss_fix(sq); }
.LBB0_77:
	s_waitcnt lgkmcnt(0)
	s_nop 1
	v_mov_b32_e32 v24, v220
	v_mov_b32_e32 v25, v221
	v_mov_b32_e32 v26, v222
	v_mov_b32_e32 v27, v223
	global_load_dwordx4 v[28:31], v[12:13], off offset:-4096
	global_load_dwordx4 v[32:35], v[12:13], off offset:-4080
	s_nop 1
	v_mov_b32_e32 v36, v224
	v_mov_b32_e32 v37, v225
	v_mov_b32_e32 v38, v226
	v_mov_b32_e32 v39, v227
	global_load_dwordx4 v[64:67], v[12:13], off offset:-2048
	global_load_dwordx4 v[68:71], v[12:13], off offset:-2032
	global_load_dwordx4 v[72:75], v[12:13], off
	global_load_dwordx4 v[76:79], v[12:13], off offset:16
	global_load_dwordx4 v[80:83], v[12:13], off offset:2048
	global_load_dwordx4 v[84:87], v[12:13], off offset:2064
	v_lshl_add_u64 v[14:15], s[52:53], 0, v[10:11]
	v_add_co_u32_e64 v14, s[0:1], s13, v14
	s_waitcnt vmcnt(2)
	v_pk_mul_f32 v[26:27], v[30:31], v[26:27]
	v_addc_co_u32_e64 v15, s[0:1], 0, v15, s[0:1]
	v_pk_mul_f32 v[24:25], v[28:29], v[24:25]
	s_waitcnt vmcnt(0)
	v_pk_mul_f32 v[38:39], v[34:35], v[38:39]
	v_pk_mul_f32 v[36:37], v[32:33], v[36:37]
	v_cvt_pk_bf16_f32 v24, v24, v25
	v_cvt_pk_bf16_f32 v25, v26, v27
	v_mul_f32_e32 v29, v29, v29
	v_cvt_pk_bf16_f32 v26, v36, v37
	v_cvt_pk_bf16_f32 v27, v38, v39
	global_store_dwordx4 v[14:15], v[24:27], off
	s_nop 1
	v_mov_b32_e32 v24, v228
	v_mov_b32_e32 v25, v229
	v_mov_b32_e32 v26, v230
	v_mov_b32_e32 v27, v231
	s_nop 0
	s_nop 1
	v_mov_b32_e32 v36, v64
	v_mov_b32_e32 v37, v65
	v_mov_b32_e32 v38, v66
	v_mov_b32_e32 v39, v67
	s_nop 1
	v_mov_b32_e32 v40, v68
	v_mov_b32_e32 v41, v69
	v_mov_b32_e32 v42, v70
	v_mov_b32_e32 v43, v71
	s_nop 1
	v_mov_b32_e32 v44, v232
	v_mov_b32_e32 v45, v233
	v_mov_b32_e32 v46, v234
	v_mov_b32_e32 v47, v235
	v_mul_f32_e32 v31, v31, v31
	v_fmac_f32_e32 v29, v28, v28
	v_fmac_f32_e32 v31, v30, v30
	v_add_f32_e32 v28, v29, v31
	v_mul_f32_e32 v33, v33, v33
	v_mul_f32_e32 v35, v35, v35
	v_fmac_f32_e32 v33, v32, v32
	v_fmac_f32_e32 v35, v34, v34
	v_add_f32_e32 v28, v28, v33
	v_add_f32_e32 v28, v35, v28
	v_cmp_lt_i32_e64 s[0:1], v17, v16
	s_nop 0
	v_pk_mul_f32 v[26:27], v[38:39], v[26:27]
	v_pk_mul_f32 v[24:25], v[36:37], v[24:25]
	s_nop 0
	v_pk_mul_f32 v[46:47], v[42:43], v[46:47]
	v_pk_mul_f32 v[44:45], v[40:41], v[44:45]
	v_cvt_pk_bf16_f32 v24, v24, v25
	v_cvt_pk_bf16_f32 v25, v26, v27
	v_mul_f32_e32 v29, v37, v37
	v_cvt_pk_bf16_f32 v26, v44, v45
	v_cvt_pk_bf16_f32 v27, v46, v47
	global_store_dwordx4 v[14:15], v[24:27], off offset:1024
	s_nop 1
	v_mov_b32_e32 v24, v236
	v_mov_b32_e32 v25, v237
	v_mov_b32_e32 v26, v238
	v_mov_b32_e32 v27, v239
	s_nop 0
	s_nop 1
	v_mov_b32_e32 v44, v72
	v_mov_b32_e32 v45, v73
	v_mov_b32_e32 v46, v74
	v_mov_b32_e32 v47, v75
	s_nop 1
	v_mov_b32_e32 v48, v76
	v_mov_b32_e32 v49, v77
	v_mov_b32_e32 v50, v78
	v_mov_b32_e32 v51, v79
	s_nop 1
	v_mov_b32_e32 v52, v240
	v_mov_b32_e32 v53, v241
	v_mov_b32_e32 v54, v242
	v_mov_b32_e32 v55, v243
	v_mul_f32_e32 v30, v39, v39
	v_mul_f32_e32 v31, v41, v41
	v_fmac_f32_e32 v29, v36, v36
	v_fmac_f32_e32 v30, v38, v38
	v_mul_f32_e32 v32, v43, v43
	v_fmac_f32_e32 v31, v40, v40
	v_add_f32_e32 v29, v29, v30
	v_fmac_f32_e32 v32, v42, v42
	v_add_f32_e32 v29, v29, v31
	v_add_f32_e32 v29, v32, v29
	v_add_f32_e32 v28, v28, v29
	v_cndmask_b32_e64 v23, v2, v17, s[0:1]
	v_lshlrev_b32_e32 v23, 2, v23
	v_cmp_lt_i32_e64 s[0:1], v18, v16
	s_nop 0
	v_pk_mul_f32 v[26:27], v[46:47], v[26:27]
	v_pk_mul_f32 v[24:25], v[44:45], v[24:25]
	s_nop 0
	v_pk_mul_f32 v[54:55], v[50:51], v[54:55]
	v_pk_mul_f32 v[52:53], v[48:49], v[52:53]
	v_cvt_pk_bf16_f32 v24, v24, v25
	v_cvt_pk_bf16_f32 v25, v26, v27
	v_mul_f32_e32 v29, v45, v45
	v_cvt_pk_bf16_f32 v26, v52, v53
	v_cvt_pk_bf16_f32 v27, v54, v55
	global_store_dwordx4 v[14:15], v[24:27], off offset:2048
	s_nop 1
	v_mov_b32_e32 v24, v80
	v_mov_b32_e32 v25, v81
	v_mov_b32_e32 v26, v82
	v_mov_b32_e32 v27, v83
	s_nop 0
	s_nop 1
	v_mov_b32_e32 v52, v84
	v_mov_b32_e32 v53, v85
	v_mov_b32_e32 v54, v86
	v_mov_b32_e32 v55, v87
	s_nop 1
	v_mov_b32_e32 v56, v248
	v_mov_b32_e32 v57, v249
	v_mov_b32_e32 v58, v250
	v_mov_b32_e32 v59, v251
	s_nop 1
	v_mov_b32_e32 v60, v252
	v_mov_b32_e32 v61, v253
	v_mov_b32_e32 v62, v254
	v_mov_b32_e32 v63, v255
	v_mul_f32_e32 v30, v47, v47
	v_mul_f32_e32 v31, v49, v49
	v_fmac_f32_e32 v29, v44, v44
	v_fmac_f32_e32 v30, v46, v46
	v_mul_f32_e32 v32, v51, v51
	v_fmac_f32_e32 v31, v48, v48
	v_add_f32_e32 v29, v29, v30
	v_fmac_f32_e32 v32, v50, v50
	v_add_f32_e32 v29, v29, v31
	v_add_f32_e32 v29, v32, v29
	v_add_f32_e32 v28, v28, v29
	s_nop 0
	v_mul_f32_e32 v29, v25, v25
	v_mul_f32_e32 v30, v27, v27
	s_nop 0
	v_mul_f32_e32 v31, v53, v53
	v_fmac_f32_e32 v29, v24, v24
	v_fmac_f32_e32 v30, v26, v26
	v_mul_f32_e32 v32, v55, v55
	v_fmac_f32_e32 v31, v52, v52
	v_add_f32_e32 v29, v29, v30
	v_fmac_f32_e32 v32, v54, v54
	v_add_f32_e32 v29, v29, v31
	v_add_f32_e32 v29, v32, v29
	v_add_f32_e32 v28, v28, v29
	ds_bpermute_b32 v23, v23, v28
	v_cndmask_b32_e64 v29, v2, v18, s[0:1]
	v_lshlrev_b32_e32 v29, 2, v29
	v_cmp_lt_i32_e64 s[0:1], v19, v16
	s_nop 0
	v_pk_mul_f32 v[24:25], v[24:25], v[56:57]
	s_waitcnt lgkmcnt(0)
	v_add_f32_e32 v23, v28, v23
	ds_bpermute_b32 v28, v29, v23
	v_cndmask_b32_e64 v29, v2, v19, s[0:1]
	v_lshlrev_b32_e32 v29, 2, v29
	v_cmp_lt_i32_e64 s[0:1], v20, v16
	s_nop 0
	v_pk_mul_f32 v[32:33], v[52:53], v[60:61]
	s_waitcnt lgkmcnt(0)
	v_add_f32_e32 v23, v23, v28
	ds_bpermute_b32 v28, v29, v23
	v_cndmask_b32_e64 v29, v2, v20, s[0:1]
	v_lshlrev_b32_e32 v29, 2, v29
	v_cmp_lt_i32_e64 s[0:1], v21, v16
	s_waitcnt lgkmcnt(0)
	v_add_f32_e32 v23, v23, v28
	ds_bpermute_b32 v31, v29, v23
	v_cndmask_b32_e64 v30, v2, v21, s[0:1]
	v_lshlrev_b32_e32 v30, 2, v30
	v_pk_mul_f32 v[28:29], v[26:27], v[58:59]
	v_cmp_lt_i32_e64 s[0:1], v22, v16
	s_waitcnt lgkmcnt(0)
	v_add_f32_e32 v23, v23, v31
	ds_bpermute_b32 v27, v30, v23
	v_cndmask_b32_e64 v34, v2, v22, s[0:1]
	v_cvt_pk_bf16_f32 v26, v24, v25
	v_lshlrev_b32_e32 v24, 2, v34
	v_pk_mul_f32 v[30:31], v[54:55], v[62:63]
	s_waitcnt lgkmcnt(0)
	v_add_f32_e32 v23, v23, v27
	ds_bpermute_b32 v24, v24, v23
	v_cvt_pk_bf16_f32 v27, v28, v29
	v_cvt_pk_bf16_f32 v28, v32, v33
	v_cvt_pk_bf16_f32 v29, v30, v31
	global_store_dwordx4 v[14:15], v[26:29], off offset:3072
	s_and_saveexec_b64 s[0:1], vcc
	s_cbranch_execz .LBB0_76
	s_waitcnt lgkmcnt(0)
	v_add_f32_e32 v14, v23, v24
	v_mul_f32_e32 v14, 0x4b800000, v14
	v_trunc_f32_e32 v14, v14
	v_mul_f32_e32 v15, 0x2f800000, v14
	v_floor_f32_e32 v15, v15
	v_fmac_f32_e32 v14, 0xcf800000, v15
	v_cvt_u32_f32_e32 v14, v14
	v_cvt_u32_f32_e32 v15, v15
	s_add_u32 s34, s52, s3
	s_addc_u32 s35, s53, s12
	global_store_dwordx2 v3, v[14:15], s[34:35]
	s_branch .LBB0_76
